# baseline (speedup 1.0000x reference)
_Z11gram_kernelPKfPKiS0_S0_S0_S0_S0_S0_S0_S0_S0_Pf:
	s_load_dwordx4 s[24:27], s[0:1], 0x0
	s_load_dwordx2 s[28:29], s[0:1], 0x40
	s_load_dwordx4 s[20:23], s[0:1], 0x30
	s_load_dwordx2 s[10:11], s[0:1], 0x58
	s_load_dwordx2 s[44:45], s[0:1], 0x20
	s_load_dwordx2 s[68:69], s[0:1], 0x10
	s_load_dwordx2 s[60:61], s[0:1], 0x18
	s_load_dwordx2 s[62:63], s[0:1], 0x28
	s_load_dwordx2 s[64:65], s[0:1], 0x48
	s_load_dwordx2 s[66:67], s[0:1], 0x50
	s_ashr_i32 s30, s2, 1
	v_mov_b32_e32 v11, 0
	s_ashr_i32 s31, s30, 31
	s_lshl_b32 s46, s30, 11
	s_lshl_b32 s3, s2, 10
	s_ashr_i32 s47, s46, 31
	s_and_b32 s33, s3, 0x400
	v_lshlrev_b32_e32 v46, 2, v0
	v_mov_b32_e32 v47, 0
	v_lshlrev_b32_e32 v212, 1, v0
	v_mov_b32_e32 v213, v47
	v_lshrrev_b32_e32 v219, 6, v0
	v_bfe_u32 v214, v0, 5, 1
	v_and_b32_e32 v220, 31, v0
	s_or_b32 s3, s46, s33
	v_lshlrev_b32_e32 v216, 4, v219
	v_lshlrev_b32_e32 v221, 3, v214
	v_or3_b32 v1, s3, v216, v221
	v_lshlrev_b32_e32 v232, 4, v220
	v_and_b32_e32 v218, 63, v0
	s_mov_b32 s39, 0x20000
	s_brev_b32 s38, 16
	v_lshl_or_b32 v180, v1, 9, v232
	v_add_u32_e32 v1, 0x10000, v180
	s_lshl_b64 s[4:5], s[46:47], 2
	s_lshl_b32 s3, s33, 2
	v_lshrrev_b32_e32 v2, 5, v0
	v_lshl_or_b32 v2, v2, 12, v232
	v_lshlrev_b32_e32 v247, 2, v46
	v_add_u32_e32 v3, 0x2000, v247
	v_and_b32_e32 v4, 0xffffff80, v0
	v_lshl_add_u32 v4, v214, 4, v4
	s_lshl_b64 s[6:7], s[30:31], 14
	s_waitcnt lgkmcnt(0)
	s_load_dword s71, s[66:67], 0x0
	s_add_u32 s48, s20, s6
	s_addc_u32 s49, s21, s7
	s_mov_b64 s[36:37], s[24:25]
	s_and_b32 s37, s37, 0xffff
	s_add_u32 s26, s26, s4
	s_addc_u32 s27, s27, s5
	s_add_u32 s26, s26, s3
	s_addc_u32 s27, s27, 0
	v_lshl_add_u64 v[32:33], v[212:213], 2, s[26:27]
	global_load_dwordx2 v[32:33], v[32:33], off
	buffer_load_dwordx4 v[34:37], v180, s[36:39], 0 offen nt
	buffer_load_dwordx4 v[38:41], v180, s[36:39], 0 offen offset:512 nt
	buffer_load_dwordx4 v[42:45], v180, s[36:39], 0 offen offset:1024 nt
	buffer_load_dwordx4 v[96:99], v180, s[36:39], 0 offen offset:1536 nt
	buffer_load_dwordx4 v[100:103], v180, s[36:39], 0 offen offset:2048 nt
	buffer_load_dwordx4 v[104:107], v180, s[36:39], 0 offen offset:2560 nt
	buffer_load_dwordx4 v[108:111], v180, s[36:39], 0 offen offset:3072 nt
	buffer_load_dwordx4 v[112:115], v180, s[36:39], 0 offen offset:3584 nt
	global_load_dword v237, v47, s[28:29]
	global_load_dword v237, v47, s[68:69]
	global_load_dword v237, v47, s[44:45]
	global_load_dword v237, v47, s[60:61]
	global_load_dword v237, v47, s[62:63]
	global_load_dwordx4 v[148:151], v2, s[22:23]
	global_load_dwordx4 v[152:155], v2, s[22:23] offset:512
	global_load_dwordx4 v[156:159], v2, s[22:23] offset:1024
	global_load_dwordx4 v[160:163], v2, s[22:23] offset:1536
	global_load_dwordx4 v[164:167], v2, s[22:23] offset:2048
	global_load_dwordx4 v[168:171], v2, s[22:23] offset:2560
	global_load_dwordx4 v[172:175], v2, s[22:23] offset:3072
	global_load_dwordx4 v[176:179], v2, s[22:23] offset:3584
	global_load_dwordx4 v[204:207], v247, s[48:49]
	global_load_dwordx4 v[208:211], v3, s[48:49]
	global_load_dwordx4 v[188:191], v4, s[64:65]
	global_load_dwordx4 v[192:195], v4, s[64:65] offset:32
	global_load_dwordx4 v[196:199], v4, s[64:65] offset:64
	global_load_dwordx4 v[200:203], v4, s[64:65] offset:96
	buffer_load_dwordx4 v[116:119], v1, s[36:39], 0 offen nt
	buffer_load_dwordx4 v[120:123], v1, s[36:39], 0 offen offset:512 nt
	buffer_load_dwordx4 v[124:127], v1, s[36:39], 0 offen offset:1024 nt
	buffer_load_dwordx4 v[128:131], v1, s[36:39], 0 offen offset:1536 nt
	buffer_load_dwordx4 v[132:135], v1, s[36:39], 0 offen offset:2048 nt
	buffer_load_dwordx4 v[136:139], v1, s[36:39], 0 offen offset:2560 nt
	buffer_load_dwordx4 v[140:143], v1, s[36:39], 0 offen offset:3072 nt
	buffer_load_dwordx4 v[144:147], v1, s[36:39], 0 offen offset:3584 nt
	s_movk_i32 s3, 0x160
	v_cmp_gt_u32_e32 vcc, s3, v0
	s_mov_b32 s3, 0x10000
	v_lshrrev_b32_e32 v227, 5, v0
	v_and_b32_e32 v228, 0x7c, v46
	v_add_u32_e32 v2, 0x200, v0
	v_lshrrev_b32_e32 v229, 5, v2
	v_mul_u32_u24_e32 v246, 0x110, v227
	v_lshl_add_u32 v246, v220, 3, v246
	v_add_u32_e32 v246, 0x10000, v246
	s_waitcnt vmcnt(35)
	v_cmp_ne_u32_e64 s[6:7], 0, v32
	v_cmp_ne_u32_e64 s[4:5], 0, v33
	v_cmp_eq_u32_e64 s[8:9], 0, v218
	s_nop 0
	s_and_saveexec_b64 s[12:13], s[8:9]
	s_cbranch_execz .LBB0_6
	s_bcnt1_i32_b64 s6, s[6:7]
	s_bcnt1_i32_b64 s4, s[4:5]
	v_mov_b32_e32 v1, 0x21100
	s_add_i32 s4, s4, s6
	v_lshl_add_u32 v1, v219, 2, v1
	v_mov_b32_e32 v2, s4
	ds_write_b32 v1, v2
.LBB0_6:
	s_or_b64 exec, exec, s[12:13]
	v_lshrrev_b32_e32 v222, 7, v0
	v_lshlrev_b32_e32 v215, 5, v222
	v_or_b32_e32 v231, v215, v220
	v_mul_u32_u24_e32 v224, 0x110, v231
	v_lshlrev_b32_e32 v223, 1, v221
	v_bfe_u32 v225, v0, 6, 1
	s_waitcnt lgkmcnt(0)
	s_barrier
	v_lshlrev_b32_e32 v230, 7, v225
	v_mov_b32_e32 v1, 0x21100
	v_mov_b32_e32 v2, 0x21110
	ds_read_b128 v[6:9], v1
	ds_read_b128 v[2:5], v2
	s_mul_i32 s4, s2, 0x4590
	s_mul_hi_i32 s3, s2, 0x4590
	s_add_u32 s34, s10, s4
	s_addc_u32 s35, s11, s3
	s_and_saveexec_b64 s[4:5], vcc
	s_cbranch_execz .LBB0_8
	v_mov_b32_e32 v1, 0
	v_lshl_add_u64 v[12:13], v[0:1], 2, s[34:35]
	v_add_co_u32_e32 v12, vcc, 0x4000, v12
	s_nop 1
	v_addc_co_u32_e32 v13, vcc, 0, v13, vcc
	global_store_dword v[12:13], v11, off offset:16
.LBB0_8:
	s_or_b64 exec, exec, s[4:5]
	s_waitcnt lgkmcnt(1)
	v_add_u32_e32 v1, v7, v6
	v_add_u32_e32 v1, v1, v8
	v_add_u32_e32 v1, v1, v9
	s_waitcnt lgkmcnt(0)
	v_add_u32_e32 v1, v1, v2
	v_add_u32_e32 v1, v1, v3
	v_add_u32_e32 v1, v1, v4
	v_add_u32_e32 v226, v1, v5
	s_waitcnt vmcnt(8)
	v_mul_u32_u24_e32 v5, 0x880, v227
	v_lshl_add_u32 v5, v220, 3, v5
	v_add_u32_e32 v5, 0x10000, v5
	v_cvt_pk_f16_f32 v6, v148, v149
	v_cvt_pk_f16_f32 v7, v150, v151
	v_cvt_pk_f16_f32 v8, v152, v153
	v_cvt_pk_f16_f32 v9, v154, v155
	ds_write2_b64 v5, v[6:7], v[8:9] offset1:34
	v_cvt_pk_f16_f32 v12, v156, v157
	v_cvt_pk_f16_f32 v13, v158, v159
	v_cvt_pk_f16_f32 v14, v160, v161
	v_cvt_pk_f16_f32 v15, v162, v163
	ds_write2_b64 v5, v[12:13], v[14:15] offset0:68 offset1:102
	v_cvt_pk_f16_f32 v6, v164, v165
	v_cvt_pk_f16_f32 v7, v166, v167
	v_cvt_pk_f16_f32 v8, v168, v169
	v_cvt_pk_f16_f32 v9, v170, v171
	ds_write2_b64 v5, v[6:7], v[8:9] offset0:136 offset1:170
	v_cvt_pk_f16_f32 v12, v172, v173
	v_cvt_pk_f16_f32 v13, v174, v175
	v_cvt_pk_f16_f32 v14, v176, v177
	v_cvt_pk_f16_f32 v15, v178, v179
	ds_write2_b64 v5, v[12:13], v[14:15] offset0:204 offset1:238
	v_mul_u32_u24_e32 v10, 0x110, v227
	v_lshl_add_u32 v10, v220, 3, v10
	v_add_u32_e32 v10, 0x18800, v10
	v_cvt_pk_f16_f32 v6, v204, v205
	v_cvt_pk_f16_f32 v7, v206, v207
	ds_write_b64 v10, v[6:7]
	v_cvt_pk_f16_f32 v8, v208, v209
	v_cvt_pk_f16_f32 v9, v210, v211
	ds_write_b64 v10, v[8:9] offset:4352
	v_readfirstlane_b32 s70, v225
	s_waitcnt lgkmcnt(0)
	s_barrier
	s_cmp_lg_u32 s70, 0
	s_cbranch_scc1 .Lqt_done
	v_add_u32_e32 v5, v224, v223
	v_add_u32_e32 v5, 0x10000, v5
	v_mul_u32_u24_e32 v10, 0x110, v220
	v_add_u32_e32 v10, v10, v223
	v_add_u32_e32 v10, 0x18800, v10
	ds_read_b128 v[48:51], v5
	ds_read_b128 v[80:83], v10
	ds_read_b128 v[52:55], v5 offset:32
	ds_read_b128 v[84:87], v10 offset:32
	ds_read_b128 v[56:59], v5 offset:64
	ds_read_b128 v[88:91], v10 offset:64
	ds_read_b128 v[60:63], v5 offset:96
	ds_read_b128 v[92:95], v10 offset:96
	ds_read_b128 v[64:67], v5 offset:128
	ds_read_b128 v[204:207], v10 offset:128
	ds_read_b128 v[68:71], v5 offset:160
	ds_read_b128 v[208:211], v10 offset:160
	ds_read_b128 v[72:75], v5 offset:192
	ds_read_b128 v[234:237], v10 offset:192
	ds_read_b128 v[76:79], v5 offset:224
	ds_read_b128 v[238:241], v10 offset:224
	v_div_scale_f32 v12, s[72:73], s71, s71, 1.0
	v_rcp_f32_e32 v14, v12
	v_div_scale_f32 v13, vcc, 1.0, s71, 1.0
	s_waitcnt lgkmcnt(14)
	v_mfma_f32_32x32x16_f16 v[188:203], v[48:51], v[80:83], v[188:203]
	v_fma_f32 v15, -v12, v14, 1.0
	v_fmac_f32_e32 v14, v15, v14
	v_mul_f32_e32 v15, v13, v14
	s_waitcnt lgkmcnt(12)
	v_mfma_f32_32x32x16_f16 v[188:203], v[52:55], v[84:87], v[188:203]
	v_fma_f32 v16, -v12, v15, v13
	v_fmac_f32_e32 v15, v16, v14
	s_waitcnt lgkmcnt(10)
	v_mfma_f32_32x32x16_f16 v[188:203], v[56:59], v[88:91], v[188:203]
	v_fma_f32 v16, -v12, v15, v13
	v_div_fmas_f32 v16, v16, v14, v15
	s_waitcnt lgkmcnt(8)
	v_mfma_f32_32x32x16_f16 v[188:203], v[60:63], v[92:95], v[188:203]
	v_div_fixup_f32 v16, v16, s71, 1.0
	s_waitcnt lgkmcnt(6)
	v_mfma_f32_32x32x16_f16 v[188:203], v[64:67], v[204:207], v[188:203]
	s_waitcnt lgkmcnt(4)
	v_mfma_f32_32x32x16_f16 v[188:203], v[68:71], v[208:211], v[188:203]
	s_waitcnt lgkmcnt(2)
	v_mfma_f32_32x32x16_f16 v[188:203], v[72:75], v[234:237], v[188:203]
	s_waitcnt lgkmcnt(0)
	v_mfma_f32_32x32x16_f16 v[188:203], v[76:79], v[238:241], v[188:203]
	s_nop 11
	v_mul_f32_e32 v17, v16, v188
	v_mul_f32_e32 v18, v16, v189
	v_mul_f32_e32 v19, v16, v190
	v_mul_f32_e32 v20, v16, v191
	v_mul_f32_e32 v21, v16, v192
	v_mul_f32_e32 v22, v16, v193
	v_mul_f32_e32 v23, v16, v194
	v_mul_f32_e32 v24, v16, v195
	v_mul_f32_e32 v25, v16, v196
	v_mul_f32_e32 v26, v16, v197
	v_mul_f32_e32 v27, v16, v198
	v_mul_f32_e32 v28, v16, v199
	v_mul_f32_e32 v29, v16, v200
	v_mul_f32_e32 v30, v16, v201
	v_mul_f32_e32 v31, v16, v202
	v_mul_f32_e32 v32, v16, v203
	v_cvt_pk_f16_f32 v248, v17, v18
	v_cvt_pk_f16_f32 v249, v19, v20
	v_cvt_pk_f16_f32 v250, v21, v22
	v_cvt_pk_f16_f32 v251, v23, v24
	v_cvt_pk_f16_f32 v252, v25, v26
	v_cvt_pk_f16_f32 v253, v27, v28
	v_cvt_pk_f16_f32 v254, v29, v30
	v_cvt_pk_f16_f32 v255, v31, v32
.Lqt_done:
	s_movk_i32 s3, 0x400
	v_cmp_gt_i32_e64 s[8:9], s3, v226
	s_movk_i32 s3, 0x3ff
	v_cmp_lt_i32_e32 vcc, s3, v226
	s_movk_i32 s3, 0x100
	v_cmp_gt_u32_e64 s[4:5], s3, v0
	s_movk_i32 s3, 0xff
	s_and_b32 s41, s23, 0xffff
	s_and_b32 s29, s29, 0xffff
	s_mov_b32 s43, 0x20000
	s_mov_b32 s42, 0x10000
	v_lshl_or_b32 v1, v227, 12, v232
	v_cmp_lt_u32_e64 s[6:7], s3, v0
	s_cbranch_vccz .LBB0_18
	s_and_saveexec_b64 s[10:11], s[6:7]
	s_xor_b64 s[10:11], exec, s[10:11]
	s_cbranch_execz .LBB0_13
	v_lshlrev_b32_e32 v3, 4, v218
	v_lshlrev_b32_e32 v4, 4, v0
	s_movk_i32 s3, 0xc00
	v_and_b32_e32 v2, 6, v222
	v_and_or_b32 v181, v4, s3, v3
	s_add_i32 s3, s46, s33
	v_lshl_or_b32 v182, v2, 10, v3
	v_add3_u32 v2, s3, v216, v221
	v_lshl_or_b32 v2, v2, 9, v232
	v_add_u32_e32 v183, 0x30000, v2
	v_mov_b32_e32 v2, 0
	v_lshl_or_b32 v180, v219, 12, v3
	s_mov_b32 s3, -2
	s_brev_b32 s16, 16
	s_mov_b32 s17, 0x10000
	s_waitcnt vmcnt(13)
	v_mov_b32_e32 v167, v45
	v_mov_b32_e32 v166, v44
	v_mov_b32_e32 v165, v43
	v_mov_b32_e32 v164, v42
	v_mov_b32_e32 v155, v41
	v_mov_b32_e32 v154, v40
	v_mov_b32_e32 v153, v39
	v_mov_b32_e32 v152, v38
	v_mov_b32_e32 v151, v37
	v_mov_b32_e32 v150, v36
	v_mov_b32_e32 v149, v35
	v_mov_b32_e32 v148, v34
	s_waitcnt vmcnt(12)
	v_mov_b32_e32 v156, v96
	v_mov_b32_e32 v157, v97
	v_mov_b32_e32 v158, v98
	v_mov_b32_e32 v159, v99
	s_waitcnt vmcnt(11)
	v_mov_b32_e32 v160, v100
	v_mov_b32_e32 v161, v101
	v_mov_b32_e32 v162, v102
	v_mov_b32_e32 v163, v103
	s_waitcnt vmcnt(10)
	v_mov_b32_e32 v168, v104
	v_mov_b32_e32 v169, v105
	v_mov_b32_e32 v170, v106
	v_mov_b32_e32 v171, v107
	s_waitcnt vmcnt(9)
	v_mov_b32_e32 v172, v108
	v_mov_b32_e32 v173, v109
	v_mov_b32_e32 v174, v110
	v_mov_b32_e32 v175, v111
	s_waitcnt vmcnt(8)
	v_mov_b32_e32 v176, v112
	v_mov_b32_e32 v177, v113
	v_mov_b32_e32 v178, v114
	v_mov_b32_e32 v179, v115
	v_mov_b32_e32 v3, v2
	v_mov_b32_e32 v4, v2
	v_mov_b32_e32 v5, v2
	v_mov_b32_e32 v6, v2
	v_mov_b32_e32 v7, v2
	v_mov_b32_e32 v8, v2
	v_mov_b32_e32 v9, v2
	v_mov_b32_e32 v10, v2
	v_mov_b32_e32 v11, v2
	v_mov_b32_e32 v12, v2
	v_mov_b32_e32 v13, v2
	v_mov_b32_e32 v14, v2
	v_mov_b32_e32 v15, v2
	v_mov_b32_e32 v16, v2
	v_mov_b32_e32 v17, v2
	v_mov_b32_e32 v18, v2
	v_mov_b32_e32 v19, v2
	v_mov_b32_e32 v20, v2
	v_mov_b32_e32 v21, v2
	v_mov_b32_e32 v22, v2
	v_mov_b32_e32 v23, v2
	v_mov_b32_e32 v24, v2
	v_mov_b32_e32 v25, v2
	v_mov_b32_e32 v26, v2
	v_mov_b32_e32 v27, v2
	v_mov_b32_e32 v28, v2
	v_mov_b32_e32 v29, v2
	v_mov_b32_e32 v30, v2
	v_mov_b32_e32 v31, v2
	v_mov_b32_e32 v32, v2
	v_mov_b32_e32 v33, v2

.Lw47_xdone:
	s_waitcnt lgkmcnt(0)
	s_barrier
	s_cmp_lg_u32 s3, 2
	s_cbranch_scc1 .Lw47_ydone
	v_add_u32_e32 v201, v224, v223
	v_add_u32_e32 v201, 0x10000, v201
	v_mul_u32_u24_e32 v202, 0x110, v231
	v_add_u32_e32 v202, v202, v230
	v_or_b32_e32 v202, v202, v221
	v_add_u32_e32 v202, 0x18800, v202
	ds_read_b128 v[92:95], v201
	ds_read_b128 v[88:91], v201 offset:32
	ds_read_b128 v[84:87], v201 offset:64
	ds_read_b128 v[80:83], v201 offset:96
	ds_read_b128 v[76:79], v201 offset:128
	ds_read_b128 v[72:75], v201 offset:160
	ds_read_b128 v[68:71], v201 offset:192
	ds_read_b128 v[64:67], v201 offset:224
	ds_read2_b64 v[60:63], v202 offset1:2
	ds_read2_b64 v[56:59], v202 offset0:4 offset1:6
	ds_read2_b64 v[52:55], v202 offset0:8 offset1:10
	ds_read2_b64 v[48:51], v202 offset0:12 offset1:14
	s_waitcnt lgkmcnt(0)

.LBB0_16:
	s_cmp_gt_u32 s3, 4
	s_cselect_b64 vcc, -1, 0
	v_add_u32_e32 v180, 0xffff0000, v236
	s_and_b64 s[12:13], vcc, exec
	v_cndmask_b32_e32 v196, v180, v1, vcc
	s_cselect_b32 s13, s29, s37
	s_cselect_b32 s12, s28, s36
	s_cselect_b32 s15, 0x20000, 0x20000
	s_cselect_b32 s14, s16, 0x8000000
	s_waitcnt lgkmcnt(0)
	s_barrier
	s_cmp_lg_u32 s3, 2
	s_cbranch_scc1 .Lw03_ydone
	v_add_u32_e32 v238, v224, v223
	v_add_u32_e32 v238, 0x10000, v238
	v_mul_u32_u24_e32 v239, 0x110, v231
	v_add_u32_e32 v239, v239, v230
	v_or_b32_e32 v239, v239, v221
	v_add_u32_e32 v239, 0x18800, v239
	ds_read_b128 v[92:95], v238
	ds_read_b128 v[88:91], v238 offset:32
	ds_read_b128 v[84:87], v238 offset:64
	ds_read_b128 v[80:83], v238 offset:96
	ds_read_b128 v[76:79], v238 offset:128
	ds_read_b128 v[72:75], v238 offset:160
	ds_read_b128 v[68:71], v238 offset:192
	ds_read_b128 v[64:67], v238 offset:224
	ds_read2_b64 v[60:63], v239 offset1:2
	ds_read2_b64 v[56:59], v239 offset0:4 offset1:6
	ds_read2_b64 v[52:55], v239 offset0:8 offset1:10
	ds_read2_b64 v[48:51], v239 offset0:12 offset1:14
	s_waitcnt lgkmcnt(0)

.LBB0_18:
	s_barrier
	global_load_dwordx4 v[48:51], v247, s[68:69]
	global_load_dwordx4 v[80:83], v247, s[44:45]
	v_add_u32_e32 v247, 0x2000, v247
	global_load_dwordx4 v[52:55], v247, s[68:69]
	global_load_dwordx4 v[84:87], v247, s[44:45]
	v_add_u32_e32 v247, 0x2000, v247
	global_load_dwordx4 v[56:59], v247, s[68:69]
	global_load_dwordx4 v[88:91], v247, s[44:45]
	v_add_u32_e32 v247, 0x2000, v247
	global_load_dwordx4 v[60:63], v247, s[68:69]
	global_load_dwordx4 v[92:95], v247, s[44:45]
	v_add_u32_e32 v247, 0x2000, v247
	global_load_dwordx4 v[64:67], v247, s[68:69]
	global_load_dwordx4 v[2:5], v247, s[44:45]
	v_add_u32_e32 v247, 0x2000, v247
	global_load_dwordx4 v[68:71], v247, s[68:69]
	global_load_dwordx4 v[6:9], v247, s[44:45]
	v_add_u32_e32 v247, 0x2000, v247
	global_load_dwordx4 v[72:75], v247, s[68:69]
	global_load_dwordx4 v[10:13], v247, s[44:45]
	v_add_u32_e32 v247, 0x2000, v247
	global_load_dwordx4 v[76:79], v247, s[68:69]
	global_load_dwordx4 v[14:17], v247, s[44:45]
	s_waitcnt vmcnt(0)
	v_cvt_pk_f16_f32 v48, v48, v49
	v_cvt_pk_f16_f32 v49, v50, v51
	ds_write_b64 v246, v[48:49]
	v_cvt_pk_f16_f32 v80, v80, v81
	v_cvt_pk_f16_f32 v81, v82, v83
	ds_write_b64 v246, v[80:81] offset:34816
	v_cvt_pk_f16_f32 v52, v52, v53
	v_cvt_pk_f16_f32 v53, v54, v55
	ds_write_b64 v246, v[52:53] offset:4352
	v_cvt_pk_f16_f32 v84, v84, v85
	v_cvt_pk_f16_f32 v85, v86, v87
	ds_write_b64 v246, v[84:85] offset:39168
	v_cvt_pk_f16_f32 v56, v56, v57
	v_cvt_pk_f16_f32 v57, v58, v59
	ds_write_b64 v246, v[56:57] offset:8704
	v_cvt_pk_f16_f32 v88, v88, v89
	v_cvt_pk_f16_f32 v89, v90, v91
	ds_write_b64 v246, v[88:89] offset:43520
	v_cvt_pk_f16_f32 v60, v60, v61
	v_cvt_pk_f16_f32 v61, v62, v63
	ds_write_b64 v246, v[60:61] offset:13056
	v_cvt_pk_f16_f32 v92, v92, v93
	v_cvt_pk_f16_f32 v93, v94, v95
	ds_write_b64 v246, v[92:93] offset:47872
	v_cvt_pk_f16_f32 v64, v64, v65
	v_cvt_pk_f16_f32 v65, v66, v67
	ds_write_b64 v246, v[64:65] offset:17408
	v_cvt_pk_f16_f32 v2, v2, v3
	v_cvt_pk_f16_f32 v3, v4, v5
	ds_write_b64 v246, v[2:3] offset:52224
	v_cvt_pk_f16_f32 v68, v68, v69
	v_cvt_pk_f16_f32 v69, v70, v71
	ds_write_b64 v246, v[68:69] offset:21760
	v_cvt_pk_f16_f32 v6, v6, v7
	v_cvt_pk_f16_f32 v7, v8, v9
	ds_write_b64 v246, v[6:7] offset:56576
	v_cvt_pk_f16_f32 v72, v72, v73
	v_cvt_pk_f16_f32 v73, v74, v75
	ds_write_b64 v246, v[72:73] offset:26112
	v_cvt_pk_f16_f32 v10, v10, v11
	v_cvt_pk_f16_f32 v11, v12, v13
	ds_write_b64 v246, v[10:11] offset:60928
	v_cvt_pk_f16_f32 v76, v76, v77
	v_cvt_pk_f16_f32 v77, v78, v79
	ds_write_b64 v246, v[76:77] offset:30464
	v_cvt_pk_f16_f32 v14, v14, v15
	v_cvt_pk_f16_f32 v15, v16, v17
	ds_write_b64 v246, v[14:15] offset:65280
	s_waitcnt lgkmcnt(0)
	s_barrier
	v_add_u32_e32 v201, v224, v223
	v_add_u32_e32 v201, 0x10000, v201
	v_mul_u32_u24_e32 v202, 0x110, v231
	v_add_u32_e32 v202, v202, v230
	v_or_b32_e32 v202, v202, v221
	v_add_u32_e32 v202, 0x18800, v202
	ds_read_b128 v[92:95], v201
	ds_read_b128 v[88:91], v201 offset:32
	ds_read_b128 v[84:87], v201 offset:64
	ds_read_b128 v[80:83], v201 offset:96
	ds_read_b128 v[76:79], v201 offset:128
	ds_read_b128 v[72:75], v201 offset:160
	ds_read_b128 v[68:71], v201 offset:192
	ds_read_b128 v[64:67], v201 offset:224
	ds_read2_b64 v[60:63], v202 offset1:2
	ds_read2_b64 v[56:59], v202 offset0:4 offset1:6
	ds_read2_b64 v[52:55], v202 offset0:8 offset1:10
	ds_read2_b64 v[48:51], v202 offset0:12 offset1:14
	s_waitcnt lgkmcnt(0)
	s_mov_b64 s[10:11], -1
	s_branch .LBB0_20

.LBB0_35:
	s_or_b64 exec, exec, s[0:1]
	s_waitcnt vmcnt(14)
	v_mul_u32_u24_e32 v105, 0x880, v227
	s_waitcnt vmcnt(11)
	v_cvt_pk_f16_f32 v3, v150, v151
	v_cvt_pk_f16_f32 v2, v148, v149
	v_lshl_add_u32 v4, v1, 1, v105
	s_waitcnt vmcnt(10)
	v_cvt_pk_f16_f32 v1, v154, v155
	s_waitcnt lgkmcnt(0)
	v_cvt_pk_f16_f32 v0, v152, v153
	s_barrier
	v_lshl_or_b32 v233, v225, 6, v220
	v_mul_u32_u24_e32 v233, 0x110, v233
	v_add_u32_e32 v233, v233, v223
	v_add_u32_e32 v233, 0x10000, v233
	ds_read_b128 v[180:183], v233
	ds_read_b128 v[184:187], v233 offset:32
	ds_read_b128 v[188:191], v233 offset:64
	ds_read_b128 v[192:195], v233 offset:96
	ds_read_b128 v[196:199], v233 offset:128
	ds_read_b128 v[200:203], v233 offset:160
	ds_read_b128 v[204:207], v233 offset:192
	ds_read_b128 v[208:211], v233 offset:224
	s_waitcnt vmcnt(4)
	ds_read_b128 v[148:151], v233 offset:8704
	ds_read_b128 v[152:155], v233 offset:8736
	ds_read_b128 v[156:159], v233 offset:8768
	ds_read_b128 v[160:163], v233 offset:8800
	ds_read_b128 v[164:167], v233 offset:8832
	ds_read_b128 v[168:171], v233 offset:8864
	ds_read_b128 v[172:175], v233 offset:8896
	ds_read_b128 v[176:179], v233 offset:8928
	s_waitcnt vmcnt(0)
	v_mov_b32_e32 v97, 0
	v_mov_b32_e32 v0, 0
	v_mov_b32_e32 v4, 0
	v_mov_b32_e32 v96, 0
	s_and_saveexec_b64 s[0:1], vcc
	s_cbranch_execz .LBB0_37
	v_lshl_add_u32 v1, v220, 1, v230
	v_or_b32_e32 v2, 0x21000, v1
	v_add_u32_e32 v1, 0x21040, v1
	ds_read_u16 v1, v1
	ds_read_u16 v2, v2
	v_cvt_f16_f32_e32 v0, v104
	s_waitcnt lgkmcnt(1)
	v_and_b32_e32 v4, 0xffff, v1
	v_pack_b32_f16 v0, v0, 0
	s_waitcnt lgkmcnt(0)
	v_and_b32_e32 v96, 0xffff, v2
.LBB0_37:
	s_or_b64 exec, exec, s[0:1]
	v_mov_b32_e32 v98, v97
	v_mov_b32_e32 v99, v97
	v_mov_b32_e32 v5, v97
	v_mov_b32_e32 v6, v97
	v_mov_b32_e32 v7, v97
	v_mov_b32_e32 v1, v97
	v_mov_b32_e32 v2, v97
	v_mov_b32_e32 v3, v97
	s_mov_b32 s0, 0x10000
	v_or_b32_e32 v8, 0x21000, v223
	v_mfma_f32_32x32x16_f16 v[32:47], v[96:99], v[0:3], 0
	v_mfma_f32_32x32x16_f16 v[16:31], v[4:7], v[0:3], 0
	v_or_b32_e32 v114, 0x21000, v223
	v_cmp_eq_u32_e64 s[0:1], 0, v225
	s_and_b64 vcc, vcc, s[0:1]
	ds_read_b128 v[8:11], v114
	ds_read_b128 v[12:15], v114 offset:32
	ds_read_b128 v[234:237], v114 offset:64
	ds_read_b128 v[238:241], v114 offset:96
	ds_read_b128 v[242:245], v114 offset:128
	ds_read_b128 v[106:109], v114 offset:160
	ds_read_b128 v[110:113], v114 offset:192
	s_waitcnt lgkmcnt(7)
	v_mfma_f32_32x32x16_f16 v[32:47], v[180:183], v[92:95], v[32:47]
	ds_read_b128 v[0:3], v114 offset:224
	v_mfma_f32_32x32x16_f16 v[32:47], v[184:187], v[88:91], v[32:47]
	v_mfma_f32_32x32x16_f16 v[32:47], v[188:191], v[84:87], v[32:47]
	v_mfma_f32_32x32x16_f16 v[32:47], v[192:195], v[80:83], v[32:47]
	v_mfma_f32_32x32x16_f16 v[32:47], v[196:199], v[76:79], v[32:47]
	v_mfma_f32_32x32x16_f16 v[32:47], v[200:203], v[72:75], v[32:47]
	v_mfma_f32_32x32x16_f16 v[32:47], v[204:207], v[68:71], v[32:47]
	v_mfma_f32_32x32x16_f16 v[32:47], v[208:211], v[64:67], v[32:47]
	s_waitcnt lgkmcnt(0)
	v_dot2c_f32_f16_e32 v98, v92, v8
	v_mfma_f32_32x32x16_f16 v[16:31], v[148:151], v[92:95], v[16:31]
	v_dot2c_f32_f16_e32 v98, v93, v9
	v_dot2c_f32_f16_e32 v98, v94, v10
	v_dot2c_f32_f16_e32 v98, v95, v11
	v_dot2c_f32_f16_e32 v98, v88, v12
	v_mfma_f32_32x32x16_f16 v[16:31], v[152:155], v[88:91], v[16:31]
	v_dot2c_f32_f16_e32 v98, v89, v13
	v_dot2c_f32_f16_e32 v98, v90, v14
	v_dot2c_f32_f16_e32 v98, v91, v15
	v_dot2c_f32_f16_e32 v98, v84, v234
	v_mfma_f32_32x32x16_f16 v[16:31], v[156:159], v[84:87], v[16:31]
	v_dot2c_f32_f16_e32 v98, v85, v235
	v_dot2c_f32_f16_e32 v98, v86, v236
	v_dot2c_f32_f16_e32 v98, v87, v237
	v_dot2c_f32_f16_e32 v98, v80, v238
	v_mfma_f32_32x32x16_f16 v[16:31], v[160:163], v[80:83], v[16:31]
	v_dot2c_f32_f16_e32 v98, v81, v239
	v_dot2c_f32_f16_e32 v98, v82, v240
	v_dot2c_f32_f16_e32 v98, v83, v241
	v_dot2c_f32_f16_e32 v98, v76, v242
	v_mfma_f32_32x32x16_f16 v[16:31], v[164:167], v[76:79], v[16:31]
	v_dot2c_f32_f16_e32 v98, v77, v243
	v_dot2c_f32_f16_e32 v98, v78, v244
	v_dot2c_f32_f16_e32 v98, v79, v245
	v_dot2c_f32_f16_e32 v98, v72, v106
	v_mfma_f32_32x32x16_f16 v[16:31], v[168:171], v[72:75], v[16:31]
	v_dot2c_f32_f16_e32 v98, v73, v107
	v_dot2c_f32_f16_e32 v98, v74, v108
	v_dot2c_f32_f16_e32 v98, v75, v109
	v_dot2c_f32_f16_e32 v98, v68, v110
	v_mfma_f32_32x32x16_f16 v[16:31], v[172:175], v[68:71], v[16:31]
	v_dot2c_f32_f16_e32 v98, v69, v111
	v_dot2c_f32_f16_e32 v98, v70, v112
	v_dot2c_f32_f16_e32 v98, v71, v113
	v_cvt_pk_f16_f32 v7, v38, v39
	v_cvt_pk_f16_f32 v6, v36, v37
	v_cvt_pk_f16_f32 v5, v34, v35
	v_cvt_pk_f16_f32 v4, v32, v33
	v_dot2c_f32_f16_e32 v98, v64, v0
	v_dot2c_f32_f16_e32 v98, v65, v1
	v_dot2c_f32_f16_e32 v98, v66, v2
	v_mfma_f32_32x32x16_f16 v[16:31], v[176:179], v[64:67], v[16:31]
	v_dot2c_f32_f16_e32 v98, v67, v3
	v_cvt_pk_f16_f32 v35, v46, v47
	v_cvt_pk_f16_f32 v34, v44, v45
	v_cvt_pk_f16_f32 v33, v42, v43
	v_cvt_pk_f16_f32 v32, v40, v41
	ds_bpermute_b32 v36, v102, v98
	v_cvt_f32_i32_e32 v37, v226
	v_mfma_f32_32x32x16_f16 v[0:15], v[4:7], v[60:63], 0
	s_nop 3
	v_cvt_pk_f16_f32 v23, v22, v23
	v_cvt_pk_f16_f32 v22, v20, v21
	v_cvt_pk_f16_f32 v21, v18, v19
	v_cvt_pk_f16_f32 v20, v16, v17
	v_cvt_pk_f16_f32 v19, v30, v31
	v_cvt_pk_f16_f32 v18, v28, v29
	v_cvt_pk_f16_f32 v17, v26, v27
	v_mfma_f32_32x32x16_f16 v[0:15], v[32:35], v[56:59], v[0:15]
	v_cvt_pk_f16_f32 v16, v24, v25
	s_waitcnt lgkmcnt(0)
	v_add_f32_e32 v36, v98, v36
	v_cvt_f16_f32_e32 v26, v100
	v_mov_b32_e32 v98, v97
	v_lshlrev_b32_e32 v32, 6, v218
	v_mfma_f32_32x32x16_f16 v[0:15], v[20:23], v[52:55], v[0:15]
	v_fma_mixlo_f16 v20, v37, v104, v36
	v_pack_b32_f16 v20, v20, 0
	v_pack_b32_f16 v21, v26, 0
	v_cndmask_b32_e32 v96, 0, v21, vcc
	v_mfma_f32_32x32x16_f16 v[0:15], v[16:19], v[48:51], v[0:15]
	v_cndmask_b32_e32 v16, 0, v20, vcc
	v_mov_b32_e32 v17, v97
	v_mov_b32_e32 v18, v97
	v_mov_b32_e32 v19, v97
	v_cmp_ne_u32_e32 vcc, 0, v225
	s_nop 0
	v_mfma_f32_32x32x16_f16 v[0:15], v[16:19], v[96:99], v[0:15]
	s_and_saveexec_b64 s[6:7], vcc
	s_cbranch_execz .LBB0_39
	v_lshl_or_b32 v71, v222, 12, v32
	v_add_u32_e32 v71, 0x18800, v71
	s_nop 7
	ds_write_b128 v71, v[0:3]
	ds_write_b128 v71, v[4:7] offset:16
	ds_write_b128 v71, v[8:11] offset:32
	ds_write_b128 v71, v[12:15] offset:48
.LBB0_39:
	s_or_b64 exec, exec, s[6:7]
	v_cvt_pk_f16_f32 v73, v118, v119
	v_cvt_pk_f16_f32 v72, v116, v117
	v_add_u32_e32 v76, v103, v105
	v_cvt_pk_f16_f32 v75, v122, v123
	v_cvt_pk_f16_f32 v74, v120, v121
	s_waitcnt lgkmcnt(0)
	s_barrier
	ds_write2_b64 v76, v[72:73], v[74:75] offset1:34
	v_cvt_pk_f16_f32 v73, v126, v127
	v_cvt_pk_f16_f32 v72, v124, v125
	v_cvt_pk_f16_f32 v75, v130, v131
	v_cvt_pk_f16_f32 v74, v128, v129
	ds_write2_b64 v76, v[72:73], v[74:75] offset0:68 offset1:102
	v_cvt_pk_f16_f32 v73, v134, v135
	v_cvt_pk_f16_f32 v72, v132, v133
	v_cvt_pk_f16_f32 v75, v138, v139
	v_cvt_pk_f16_f32 v74, v136, v137
	ds_write2_b64 v76, v[72:73], v[74:75] offset0:136 offset1:170
	v_cvt_pk_f16_f32 v73, v142, v143
	v_cvt_pk_f16_f32 v72, v140, v141
	v_cvt_pk_f16_f32 v75, v146, v147
	v_cvt_pk_f16_f32 v74, v144, v145
	ds_write2_b64 v76, v[72:73], v[74:75] offset0:204 offset1:238
	s_and_saveexec_b64 s[6:7], s[0:1]
	s_cbranch_execz .LBB0_49
	v_mov_b32_e32 v215, 0
	v_lshl_or_b32 v32, v222, 12, v32
	v_add_u32_e32 v78, 0x18800, v32
	ds_read_b128 v[40:43], v78
	ds_read_b128 v[44:47], v78 offset:16
	ds_read_b128 v[74:77], v78 offset:32
	ds_read_b128 v[78:81], v78 offset:48
	s_waitcnt lgkmcnt(3)
	v_add_f32_e64 v32, v0, v40
	v_add_f32_e64 v33, v1, v41
	v_add_f32_e64 v0, v42, v2
	v_add_f32_e64 v1, v43, v3
	s_waitcnt lgkmcnt(2)
	v_pk_add_f32 v[2:3], v[4:5], v[44:45]
	v_pk_add_f32 v[4:5], v[46:47], v[6:7]
	s_waitcnt lgkmcnt(1)
	v_pk_add_f32 v[6:7], v[8:9], v[74:75]
	s_waitcnt lgkmcnt(0)
	v_pk_add_f32 v[8:9], v[12:13], v[78:79]
	v_cvt_pk_f16_f32 v2, v2, v3
	v_cvt_pk_f16_f32 v3, v4, v5
	v_cvt_pk_f16_f32 v1, v0, v1
	v_cvt_pk_f16_f32 v0, v32, v33
	v_add_f32_e64 v40, v76, v10
	v_add_f32_e64 v41, v77, v11
	v_add_f32_e64 v10, v80, v14
	v_add_f32_e64 v11, v81, v15
	v_cvt_pk_f16_f32 v34, v8, v9
	v_cvt_pk_f16_f32 v32, v6, v7
	v_cvt_pk_f16_f32 v35, v10, v11
	v_cvt_pk_f16_f32 v33, v40, v41
	s_andn2_b64 vcc, exec, s[8:9]
	s_nop 1
	v_mfma_f32_32x32x16_f16 v[0:15], v[0:3], v[248:251], 0
	v_mfma_f32_32x32x16_f16 v[0:15], v[32:35], v[252:255], v[0:15]
	s_cbranch_vccnz .LBB0_48
	v_lshlrev_b32_e32 v16, 7, v220
	v_lshl_or_b32 v16, v222, 12, v16
	v_mov_b32_e32 v17, v215
	s_add_i32 s33, s33, s46
	v_lshlrev_b32_e32 v22, 2, v214
	v_lshl_add_u64 v[16:17], v[16:17], 2, s[44:45]
	v_add_u32_e32 v18, s33, v214
	s_mov_b64 s[0:1], 0
	s_movk_i32 s10, 0x3fd
	v_mov_b32_e32 v23, v215
	s_branch .LBB0_43

	.amdhsa_kernel _Z11gram_kernelPKfPKiS0_S0_S0_S0_S0_S0_S0_S0_S0_Pf
		.amdhsa_group_segment_fixed_size 135456
		.amdhsa_private_segment_fixed_size 0
		.amdhsa_kernarg_size 96
		.amdhsa_user_sgpr_count 2
		.amdhsa_user_sgpr_dispatch_ptr 0
		.amdhsa_user_sgpr_queue_ptr 0
		.amdhsa_user_sgpr_kernarg_segment_ptr 1
		.amdhsa_user_sgpr_dispatch_id 0
		.amdhsa_user_sgpr_kernarg_preload_length 0
		.amdhsa_user_sgpr_kernarg_preload_offset 0
		.amdhsa_user_sgpr_private_segment_size 0
		.amdhsa_uses_dynamic_stack 0
		.amdhsa_enable_private_segment 0
		.amdhsa_system_sgpr_workgroup_id_x 1
		.amdhsa_system_sgpr_workgroup_id_y 0
		.amdhsa_system_sgpr_workgroup_id_z 0
		.amdhsa_system_sgpr_workgroup_info 0
		.amdhsa_system_vgpr_workitem_id 0
		.amdhsa_next_free_vgpr 256
		.amdhsa_next_free_sgpr 96
		.amdhsa_accum_offset 256
		.amdhsa_reserve_vcc 1
		.amdhsa_float_round_mode_32 0
		.amdhsa_float_round_mode_16_64 0
		.amdhsa_float_denorm_mode_32 3
		.amdhsa_float_denorm_mode_16_64 3
		.amdhsa_dx10_clamp 1
		.amdhsa_ieee_mode 1
		.amdhsa_fp16_overflow 0
		.amdhsa_tg_split 0
		.amdhsa_exception_fp_ieee_invalid_op 0
		.amdhsa_exception_fp_denorm_src 0
		.amdhsa_exception_fp_ieee_div_zero 0
		.amdhsa_exception_fp_ieee_overflow 0
		.amdhsa_exception_fp_ieee_underflow 0
		.amdhsa_exception_fp_ieee_inexact 0
		.amdhsa_exception_int_div_zero 0
	.end_amdhsa_kernel

amdhsa.kernels:
  - .agpr_count:     0
    .args:
      - .actual_access:  read_only
        .address_space:  global
        .offset:         0
        .size:           8
        .value_kind:     global_buffer
      - .actual_access:  read_only
        .address_space:  global
        .offset:         8
        .size:           8
        .value_kind:     global_buffer
      - .actual_access:  read_only
        .address_space:  global
        .offset:         16
        .size:           8
        .value_kind:     global_buffer
      - .actual_access:  read_only
        .address_space:  global
        .offset:         24
        .size:           8
        .value_kind:     global_buffer
      - .actual_access:  read_only
        .address_space:  global
        .offset:         32
        .size:           8
        .value_kind:     global_buffer
      - .actual_access:  read_only
        .address_space:  global
        .offset:         40
        .size:           8
        .value_kind:     global_buffer
      - .address_space:  global
        .offset:         48
        .size:           8
        .value_kind:     global_buffer
      - .address_space:  global
        .offset:         56
        .size:           8
        .value_kind:     global_buffer
      - .address_space:  global
        .offset:         64
        .size:           8
        .value_kind:     global_buffer
      - .actual_access:  read_only
        .address_space:  global
        .offset:         72
        .size:           8
        .value_kind:     global_buffer
      - .actual_access:  read_only
        .address_space:  global
        .offset:         80
        .size:           8
        .value_kind:     global_buffer
      - .actual_access:  write_only
        .address_space:  global
        .offset:         88
        .size:           8
        .value_kind:     global_buffer
    .group_segment_fixed_size: 135456
    .kernarg_segment_align: 8
    .kernarg_segment_size: 96
    .language:       OpenCL C
    .language_version:
      - 2
      - 0
    .max_flat_workgroup_size: 512
    .name:           _Z11gram_kernelPKfPKiS0_S0_S0_S0_S0_S0_S0_S0_S0_Pf
    .private_segment_fixed_size: 0
    .sgpr_count:     66
    .sgpr_spill_count: 0
    .symbol:         _Z11gram_kernelPKfPKiS0_S0_S0_S0_S0_S0_S0_S0_S0_Pf.kd
    .uniform_work_group_size: 1
    .uses_dynamic_stack: false
    .vgpr_count:     256
    .vgpr_spill_count: 0
    .wavefront_size: 64
  - .agpr_count:     0
    .args:
      - .actual_access:  read_only
        .address_space:  global
        .offset:         0
        .size:           8
        .value_kind:     global_buffer
      - .actual_access:  read_only
        .address_space:  global
        .offset:         8
        .size:           8
        .value_kind:     global_buffer
      - .actual_access:  write_only
        .address_space:  global
        .offset:         16
        .size:           8
        .value_kind:     global_buffer
    .group_segment_fixed_size: 0
    .kernarg_segment_align: 8
    .kernarg_segment_size: 24
    .language:       OpenCL C
    .language_version:
      - 2
      - 0
    .max_flat_workgroup_size: 256
    .name:           _Z10fin_kernelPKfS0_Pf
    .private_segment_fixed_size: 0
    .sgpr_count:     16
    .sgpr_spill_count: 0
    .symbol:         _Z10fin_kernelPKfS0_Pf.kd
    .uniform_work_group_size: 1
    .uses_dynamic_stack: false
    .vgpr_count:     51
    .vgpr_spill_count: 0
    .wavefront_size: 64
